# attention row-max chain: two self-max canonicalisations dropped in front of the uniform rescale test (on top of the combined variant)
# speedup vs baseline: 1.0201x; 1.0015x over previous
.LBB0_528:
	ds_read_b128 v[240:243], v233
	v_add_f32_e32 v3, v130, v131
	v_add_f32_e32 v3, v132, v3
	v_add_f32_e32 v3, v133, v3
	v_add_f32_e32 v3, v134, v3
	s_waitcnt lgkmcnt(0)
	v_mfma_f32_32x32x16_bf16 v[162:177], v[146:149], v[240:243], v[98:113]
	v_add_u32_e32 v16, s0, v223
	v_add_f32_e32 v3, v135, v3
	v_cvt_pk_bf16_f32 v194, v130, v131
	v_cvt_pk_bf16_f32 v195, v132, v133
	v_mfma_f32_32x32x16_bf16 v[146:161], v[202:205], v[240:243], v[98:113]
	v_add_f32_e32 v3, v136, v3
	v_add_f32_e32 v3, v137, v3
	v_add_f32_e32 v3, v138, v3
	v_add_f32_e32 v3, v139, v3
	v_cvt_pk_bf16_f32 v196, v134, v135
	v_cvt_pk_bf16_f32 v197, v136, v137
	ds_read_b128 v[130:133], v233 offset:1024
	v_add_f32_e32 v3, v140, v3
	v_add_f32_e32 v3, v141, v3
	v_add_f32_e32 v3, v142, v3
	v_add_f32_e32 v3, v143, v3
	s_waitcnt lgkmcnt(0)
	v_mfma_f32_32x32x16_bf16 v[162:177], v[206:209], v[130:133], v[162:177]
	v_cvt_pk_bf16_f32 v12, v138, v139
	v_cvt_pk_bf16_f32 v13, v140, v141
	v_mfma_f32_32x32x16_bf16 v[146:161], v[190:193], v[130:133], v[146:161]
	v_add_f32_e32 v3, v144, v3
	v_add_f32_e32 v3, v145, v3
	v_add_f32_e32 v3, v114, v3
	v_add_f32_e32 v3, v115, v3
	v_cvt_pk_bf16_f32 v14, v142, v143
	v_cvt_pk_bf16_f32 v15, v144, v145
	ds_read_b128 v[138:141], v233 offset:2048
	ds_read_b64_tr_b16 v[134:135], v16 offset:49152
	ds_read_b64_tr_b16 v[136:137], v16 offset:49664
	s_waitcnt lgkmcnt(2)
	v_mfma_f32_32x32x16_bf16 v[162:177], v[198:201], v[138:141], v[162:177]
	v_add_f32_e32 v3, v116, v3
	v_add_f32_e32 v3, v117, v3
	v_add_f32_e32 v3, v118, v3
	v_add_f32_e32 v3, v119, v3
	v_cvt_pk_bf16_f32 v8, v114, v115
	v_cvt_pk_bf16_f32 v9, v116, v117
	ds_read_b64_tr_b16 v[130:131], v16 offset:53248
	ds_read_b64_tr_b16 v[132:133], v16 offset:53760
	v_mfma_f32_32x32x16_bf16 v[146:161], v[186:189], v[138:141], v[146:161]
	v_add_f32_e32 v3, v120, v3
	v_add_f32_e32 v3, v121, v3
	v_add_f32_e32 v3, v122, v3
	v_add_f32_e32 v3, v123, v3
	v_cvt_pk_bf16_f32 v10, v118, v119
	v_cvt_pk_bf16_f32 v11, v120, v121
	ds_read_b128 v[138:141], v233 offset:3072
	ds_read_b64_tr_b16 v[118:119], v16 offset:57344
	ds_read_b64_tr_b16 v[120:121], v16 offset:57856
	s_waitcnt lgkmcnt(2)
	v_mfma_f32_32x32x16_bf16 v[162:177], v[182:185], v[138:141], v[162:177]
	v_add_f32_e32 v3, v124, v3
	v_add_f32_e32 v3, v125, v3
	v_add_f32_e32 v3, v126, v3
	v_add_f32_e32 v3, v127, v3
	v_cvt_pk_bf16_f32 v4, v122, v123
	v_cvt_pk_bf16_f32 v5, v124, v125
	ds_read_b64_tr_b16 v[114:115], v16 offset:61440
	ds_read_b64_tr_b16 v[116:117], v16 offset:61952
	v_mfma_f32_32x32x16_bf16 v[146:161], v[178:181], v[138:141], v[146:161]
	v_add_f32_e32 v3, v128, v3
	v_add_f32_e32 v3, v129, v3
	v_add_f32_e32 v3, 0, v3
	v_cvt_pk_bf16_f32 v6, v126, v127
	v_cvt_pk_bf16_f32 v7, v128, v129
	v_max_f32_e32 v17, v163, v163
	v_max_f32_e32 v122, v162, v162
	v_max_f32_e32 v17, v122, v17
	s_nop 3
	v_max3_f32 v122, v164, v165, v147
	v_max3_f32 v17, v17, v146, v148
	v_max3_f32 v17, v17, v149, v166
	v_max3_f32 v122, v122, v168, v169
	v_max3_f32 v17, v17, v167, v150
	v_max3_f32 v122, v122, v152, v153
	v_max3_f32 v17, v17, v151, v170
	v_max3_f32 v122, v122, v172, v173
	v_max3_f32 v17, v17, v171, v154
	v_max3_f32 v122, v122, v156, v157
	v_max3_f32 v17, v17, v155, v174
	v_max3_f32 v122, v122, v176, v177
	v_max3_f32 v17, v17, v175, v158
	v_max3_f32 v122, v122, v160, v161
	v_max3_f32 v17, v17, v159, v122
	v_mov_b32_e32 v122, v17
	s_nop 1
	v_permlane32_swap_b32_e32 v17, v122
	v_max_f32_e32 v17, v17, v122
	v_cmp_lt_f32_e32 vcc, s30, v17
	s_cmp_lg_u64 vcc, 0
	v_add_f32_e32 v3, v238, v3
	s_cselect_b64 s[0:1], -1, 0
	s_cbranch_vccnz .LBB0_536

.LBB0_531:
	ds_read_b128 v[238:241], v233
	v_add_f32_e32 v4, v162, v163
	v_add_f32_e32 v4, v164, v4
	v_add_f32_e32 v4, v165, v4
	v_add_f32_e32 v4, v166, v4
	s_waitcnt lgkmcnt(0)
	v_mfma_f32_32x32x16_bf16 v[130:145], v[114:117], v[238:241], v[98:113]
	v_add_u32_e32 v16, s57, v223
	v_add_f32_e32 v4, v167, v4
	v_cvt_pk_bf16_f32 v194, v162, v163
	v_cvt_pk_bf16_f32 v195, v164, v165
	v_mfma_f32_32x32x16_bf16 v[114:129], v[178:181], v[238:241], v[98:113]
	v_add_f32_e32 v4, v168, v4
	v_add_f32_e32 v4, v169, v4
	v_add_f32_e32 v4, v170, v4
	v_add_f32_e32 v4, v171, v4
	v_cvt_pk_bf16_f32 v196, v166, v167
	v_cvt_pk_bf16_f32 v197, v168, v169
	ds_read_b128 v[162:165], v233 offset:1024
	v_add_f32_e32 v4, v172, v4
	v_add_f32_e32 v4, v173, v4
	v_add_f32_e32 v4, v174, v4
	v_add_f32_e32 v4, v175, v4
	s_waitcnt lgkmcnt(0)
	v_mfma_f32_32x32x16_bf16 v[130:145], v[198:201], v[162:165], v[130:145]
	v_cvt_pk_bf16_f32 v12, v170, v171
	v_cvt_pk_bf16_f32 v13, v172, v173
	v_mfma_f32_32x32x16_bf16 v[114:129], v[186:189], v[162:165], v[114:129]
	v_add_f32_e32 v4, v176, v4
	v_add_f32_e32 v4, v177, v4
	v_add_f32_e32 v4, v146, v4
	v_add_f32_e32 v4, v147, v4
	v_cvt_pk_bf16_f32 v14, v174, v175
	v_cvt_pk_bf16_f32 v15, v176, v177
	ds_read_b128 v[170:173], v233 offset:2048
	ds_read_b64_tr_b16 v[166:167], v16 offset:49152
	ds_read_b64_tr_b16 v[168:169], v16 offset:49664
	s_waitcnt lgkmcnt(2)
	v_mfma_f32_32x32x16_bf16 v[130:145], v[206:209], v[170:173], v[130:145]
	v_add_f32_e32 v4, v148, v4
	v_add_f32_e32 v4, v149, v4
	v_add_f32_e32 v4, v150, v4
	v_add_f32_e32 v4, v151, v4
	v_cvt_pk_bf16_f32 v8, v146, v147
	v_cvt_pk_bf16_f32 v9, v148, v149
	ds_read_b64_tr_b16 v[162:163], v16 offset:53248
	ds_read_b64_tr_b16 v[164:165], v16 offset:53760
	v_mfma_f32_32x32x16_bf16 v[114:129], v[190:193], v[170:173], v[114:129]
	v_add_f32_e32 v4, v152, v4
	v_add_f32_e32 v4, v153, v4
	v_add_f32_e32 v4, v154, v4
	v_add_f32_e32 v4, v155, v4
	v_cvt_pk_bf16_f32 v10, v150, v151
	v_cvt_pk_bf16_f32 v11, v152, v153
	ds_read_b128 v[170:173], v233 offset:3072
	ds_read_b64_tr_b16 v[150:151], v16 offset:57344
	ds_read_b64_tr_b16 v[152:153], v16 offset:57856
	s_waitcnt lgkmcnt(2)
	v_mfma_f32_32x32x16_bf16 v[130:145], v[202:205], v[170:173], v[130:145]
	v_add_f32_e32 v4, v156, v4
	v_add_f32_e32 v4, v157, v4
	v_add_f32_e32 v4, v158, v4
	v_add_f32_e32 v17, v159, v4
	v_cvt_pk_bf16_f32 v4, v154, v155
	v_cvt_pk_bf16_f32 v5, v156, v157
	ds_read_b64_tr_b16 v[146:147], v16 offset:61440
	ds_read_b64_tr_b16 v[148:149], v16 offset:61952
	v_mfma_f32_32x32x16_bf16 v[114:129], v[182:185], v[170:173], v[114:129]
	v_add_f32_e32 v6, v160, v17
	v_add_f32_e32 v6, v161, v6
	v_add_f32_e32 v17, 0, v6
	v_cvt_pk_bf16_f32 v6, v158, v159
	v_cvt_pk_bf16_f32 v7, v160, v161
	v_max_f32_e32 v154, v131, v131
	v_max_f32_e32 v155, v130, v130
	v_max_f32_e32 v154, v155, v154
	s_nop 3
	v_max3_f32 v155, v132, v133, v115
	v_max3_f32 v154, v154, v114, v116
	v_max3_f32 v154, v154, v117, v134
	v_max3_f32 v155, v155, v136, v137
	v_max3_f32 v154, v154, v135, v118
	v_max3_f32 v155, v155, v120, v121
	v_max3_f32 v154, v154, v119, v138
	v_max3_f32 v155, v155, v140, v141
	v_max3_f32 v154, v154, v139, v122
	v_max3_f32 v155, v155, v124, v125
	v_max3_f32 v154, v154, v123, v142
	v_max3_f32 v155, v155, v144, v145
	v_max3_f32 v154, v154, v143, v126
	v_max3_f32 v155, v155, v128, v129
	v_add_f32_e32 v238, v3, v17
	v_max3_f32 v3, v154, v127, v155
	v_mov_b32_e32 v17, v3
	s_nop 1
	v_permlane32_swap_b32_e32 v3, v17
	v_max_f32_e32 v3, v3, v17
	v_cmp_lt_f32_e32 vcc, s30, v3
	s_cmp_lg_u64 vcc, 0
	s_cselect_b64 s[0:1], -1, 0
	s_cbranch_vccnz .LBB0_539
